# gathered MoBA tickets fetch their list entries together with the list length instead of after it
# speedup vs baseline: 1.0128x; 1.0049x over previous
; __device__ __forceinline__ unsigned ld_sc1(const unsigned* p) { return __hip_atomic_load(p, __ATOMIC_RELAXED, __HIP_MEMORY_SCOPE_AGENT); }
; template <int mode> __device__ __forceinline__ void attn_unit(const AttnArgs& A, const int b, const int h, const int sub, char* shm, const int wave_) {
;     ...
;     if (mode == 3) { gk = sub >> 4; const int c = sub & 15; const int li = (b * 5 + (h - 6)) * 15 + gk;
;         gcnt = __builtin_amdgcn_readfirstlane((int)ld_sc1(A.mcnt + li));
;         if (c * 256 >= gcnt) return;
;         const int gi = c * 256 + wid * 32 + r32; gvalid = gi < gcnt; wvalid = (c * 256 + wid * 32) < gcnt;
;         gent = ld_sc1(A.mlist + (size_t)li * MLCAP + (gvalid ? gi : 0)); qb = 0; }
;     const size_t rowbase = (size_t)b * SEQ + res; const int q0 = qb * 256;
;     const bf16* Qp = A.qkv + (rowbase + (size_t)dil * ((mode == 3) ? (int)(gent & 4095u) : (q0 + wid * 32 + r32))) * QS + h * 128;
;     const bf16* Kh = A.qkv + rowbase * QS + 2048 + h * 128;
;     const bf16* Vh = A.qkv + rowbase * QS + 4096 + h * 128;
;     const size_t rstep = (size_t)dil * QS;
;     char* V_lds = shm + L_V; char* K_lds = shm + L_K;
;     float* wsf = (float*)(shm + L_WS) + wid * 64; float* li_l = wsf; float* al_l = wsf + 32;
;     int* TL = (int*)(shm + L_TL); int* FLG = (int*)(shm + L_FLG); unsigned* MSK = (unsigned*)(shm + L_MSK); float* KM = (float*)(shm + L_KM);
;     char* qf = shm + L_Q + wid * 8192 + lane * 16;
;     const int qw0 = q0 + wid * 32;
;     const int pos = qw0 + r32;
;     const int vb0 = (int)(uintptr_t)V_lds + v_rd_base(lane);
;     unsigned koffb[2], voffb[2];
; #pragma unroll
;     for (int i = 0; i < 2; ++i) { const int Lb = (2 * wid + i) * 1024 + lane * 16;
;         const int rowk = Lb >> 8, ck = ((Lb >> 4) & 15) ^ (rowk & 7);
;         koffb[i] = (unsigned)(((size_t)rowk * rstep + ck * 8) * 2);
;         const int sub_ = Lb >> 9, win_ = Lb & 511, kk = (sub_ >> 2) * 8 + (win_ >> 6), kv = (kk & ~0xC) | ((kk & 4) << 1) | ((kk & 8) >> 1), cc = (sub_ & 3) * 4 + ((win_ & 63) >> 4);
;         voffb[i] = (unsigned)(((size_t)kv * rstep + cc * 8) * 2); }
;     typedef __attribute__((address_space(3))) unsigned lds_u32;
;     lds_u32* const Kdst = (lds_u32*)(K_lds + wid * 2048); lds_u32* const Vdst = (lds_u32*)(V_lds + wid * 2048);
;     ...
;     { const int kf_ = ((mode == 3) ? gk * 256 : q0) + 192; TDMA(kf_, 0); }
;     bf16x8 qr[8];
; #pragma unroll
.LBB0_516:
	s_bfe_u32 s1, s26, 0x1000b
	s_bfe_u32 s19, s26, 0x30008
	s_mul_i32 s14, s1, 5
	s_add_i32 s14, s14, s19
	s_bfe_u32 s0, s26, 0x40004
	s_mul_i32 s14, s14, 15
	s_add_i32 s14, s14, s0
	v_mbcnt_lo_u32_b32 v0, -1, 0
	v_mbcnt_hi_u32_b32 v0, -1, v0
	s_lshl_b32 s15, s14, 2
	v_readlane_b32 s16, v255, 10
	s_waitcnt vmcnt(18)
	v_add_u32_e32 v119, s94, v0
	v_mov_b32_e32 v0, s15
	v_readlane_b32 s17, v255, 11
	s_lshl_b32 s15, s26, 8
	s_and_b32 s25, s15, 0xf00
	s_nop 2
	global_load_dword v0, v0, s[16:17] sc1
	v_readlane_b32 s22, v252, 37
	v_and_b32_e32 v120, 31, v119
	s_mul_i32 s98, s14, 0x3c00
	v_readlane_b32 s16, v255, 8
	v_readlane_b32 s17, v255, 9
	s_add_i32 s22, s25, s22
	v_or_b32_e32 v116, s22, v120
	v_mov_b32_e32 v117, v1
	s_add_u32 s98, s16, s98
	s_addc_u32 s99, s17, 0
	v_lshl_add_u64 v[2:3], v[116:117], 2, s[98:99]
	global_load_dword v122, v[2:3], off sc1
	global_load_dword v117, v1, s[98:99] sc1
	s_waitcnt vmcnt(2)
	v_readfirstlane_b32 s24, v0
	s_cmp_ge_i32 s25, s24
	s_cbranch_scc1 .LBB0_666
	v_readlane_b32 s15, v252, 37
	v_and_b32_e32 v120, 31, v119
	s_add_i32 s25, s25, s15
	s_add_i32 s22, s19, 6
	v_or_b32_e32 v0, s25, v120
	s_mulk_i32 s14, 0x3c00
	v_readlane_b32 s16, v255, 8
	v_cmp_gt_i32_e64 s[40:41], s24, v0
	v_readlane_b32 s17, v255, 9
	s_add_u32 s14, s16, s14
	s_addc_u32 s15, s17, 0
	v_cndmask_b32_e64 v0, 0, v0, s[40:41]
	s_lshl_b32 s14, s1, 12
	s_lshl_b32 s18, s22, 7
	s_mul_i32 s1, s1, 0x3000000
	s_add_u32 s1, s38, s1
	s_addc_u32 s15, s39, 0
	s_lshl_b32 s30, s22, 8
	s_add_u32 s1, s1, s30
	v_and_b32_e32 v4, 63, v119
	s_addc_u32 s27, s15, 0
	v_lshlrev_b32_e32 v6, 4, v4
	v_readlane_b32 s23, v252, 28
	v_lshrrev_b32_e32 v8, 1, v119
	s_add_u32 s15, s1, 0x1000
	v_or_b32_e32 v2, s23, v6
	v_bfe_u32 v7, v119, 2, 2
	v_and_b32_e32 v8, 8, v8
	v_readlane_b32 s23, v252, 13
	s_addc_u32 s22, s27, 0
	v_and_b32_e32 v3, 15, v119
	v_or3_b32 v7, v7, v8, s23
	s_add_u32 s23, s1, 0x2000
	v_ashrrev_i32_e32 v9, 8, v2
	s_addc_u32 s27, s27, 0
	s_lshl_b32 s0, s0, 8
	v_bitop3_b32 v10, v9, v3, 3 bitop3:0x6c
	v_mul_i32_i24_e32 v9, 0x3000, v9
	s_or_b32 s28, s0, 0xc0
	v_and_b32_e32 v8, 3, v119
	v_lshl_or_b32 v125, v10, 4, v9
	v_lshrrev_b32_e32 v9, 3, v119
	s_mul_i32 s29, s28, 0x3000
	v_mul_lo_u32 v7, v7, s70
	v_and_or_b32 v9, v9, 4, v8
	v_or_b32_e32 v2, 0x400, v2
	s_add_u32 s0, s15, s29
	v_lshl_or_b32 v126, v9, 4, v7
	v_ashrrev_i32_e32 v9, 8, v2
	v_lshrrev_b32_e32 v2, 7, v2
	s_addc_u32 s1, s22, 0
	v_bitop3_b32 v3, v9, v3, 7 bitop3:0x6c
	v_mul_i32_i24_e32 v9, 0x3000, v9
	v_and_or_b32 v2, v2, 12, v8
	s_add_u32 s34, s23, s29
	v_bfe_u32 v5, v119, 5, 1
	v_lshl_or_b32 v127, v3, 4, v9
	v_lshl_or_b32 v128, v2, 4, v7
	s_mov_b32 s31, s90
	s_addc_u32 s35, s27, 0
	v_mov_b32_e32 v7, v125
	s_add_i32 m0, s2, 0x8000
	v_lshlrev_b32_e32 v114, 4, v5
	v_mov_b32_e32 v115, v1
	v_cmp_gt_i32_e32 vcc, 4, v119
	s_waitcnt vmcnt(0)
	v_cndmask_b32_e64 v122, v117, v122, s[40:41]
	v_and_b32_e32 v121, 0xfff, v122
	v_or_b32_e32 v0, s14, v121
	v_mul_u32_u24_e32 v0, 0x1800, v0
	v_lshlrev_b32_e32 v0, 1, v0
	v_lshl_add_u64 v[2:3], s[38:39], 0, v[0:1]
	v_mov_b32_e32 v0, v126
	v_lshl_add_u64 v[2:3], v[2:3], 0, s[30:31]
	global_load_lds_dwordx4 v7, s[0:1]
	s_mov_b32 m0, s2
	v_mov_b32_e32 v7, v127
	global_load_lds_dwordx4 v0, s[34:35]
	v_mov_b32_e32 v0, v128
	v_lshl_add_u64 v[2:3], v[2:3], 0, v[114:115]
	global_load_dwordx4 v[8:11], v[2:3], off
	global_load_dwordx4 v[16:19], v[2:3], off offset:32
	global_load_dwordx4 v[20:23], v[2:3], off offset:64
	global_load_dwordx4 v[24:27], v[2:3], off offset:96
	global_load_dwordx4 v[28:31], v[2:3], off offset:128
	global_load_dwordx4 v[32:35], v[2:3], off offset:160
	global_load_dwordx4 v[36:39], v[2:3], off offset:192
	global_load_dwordx4 v[40:43], v[2:3], off offset:224
	s_add_i32 m0, s2, 0x8400
	s_nop 0
	global_load_lds_dwordx4 v7, s[0:1]
	v_readlane_b32 s0, v252, 15
	s_add_i32 m0, s2, 0x400
	s_nop 0
	v_add_u32_e32 v123, s0, v6
	global_load_lds_dwordx4 v0, s[34:35]
	s_waitcnt vmcnt(0)
	ds_write_b128 v123, v[8:11]
	ds_write_b128 v123, v[16:19] offset:1024
	ds_write_b128 v123, v[20:23] offset:2048
	ds_write_b128 v123, v[24:27] offset:3072
	ds_write_b128 v123, v[28:31] offset:4096
	ds_write_b128 v123, v[32:35] offset:5120
	ds_write_b128 v123, v[36:39] offset:6144
	ds_write_b128 v123, v[40:43] offset:7168
	s_and_saveexec_b64 s[0:1], vcc
	v_lshl_add_u32 v0, v119, 2, 0
	v_lshlrev_b32_e32 v2, 6, v119
	v_add_u32_e32 v0, 0x20800, v0
	v_sub_u32_e32 v2, s28, v2
	ds_write_b32 v0, v2
	s_or_b64 exec, exec, s[0:1]
	s_cmp_lt_i32 s25, s24
	s_cselect_b64 s[24:25], -1, 0
	s_lshl_b32 s0, s19, 3
	s_sub_i32 s0, 0xffffffc8, s0
	v_cvt_f32_i32_e32 v0, s0
	s_mov_b32 s28, 0x41300000
	v_lshlrev_b32_e32 v5, 2, v5
	v_and_b32_e32 v22, 0xc0, v6
	v_div_scale_f32 v2, s[0:1], s28, s28, v0
	v_rcp_f32_e32 v3, v2
	v_div_scale_f32 v7, vcc, v0, s28, v0
	v_or_b32_e32 v6, 2, v5
	v_fma_f32 v8, -v2, v3, 1.0
	v_fmac_f32_e32 v3, v8, v3
	v_mul_f32_e32 v8, v7, v3
	v_fma_f32 v9, -v2, v8, v7
	v_fmac_f32_e32 v8, v9, v3
	v_fma_f32 v2, -v2, v8, v7
	v_div_fmas_f32 v2, v2, v3, v8
	v_div_fixup_f32 v0, v2, s28, v0
	v_exp_f32_e32 v0, v0
	v_or_b32_e32 v2, 3, v5
	v_cvt_f32_ubyte0_e32 v3, v2
	v_cvt_f32_ubyte0_e32 v2, v6
	v_mul_f32_e32 v118, 0x3fb8aa3b, v0
	v_lshlrev_b32_e32 v21, 1, v4
	v_or_b32_e32 v0, 1, v5
	v_pk_mul_f32 v[68:69], v[118:119], v[2:3] op_sel_hi:[0,1]
	v_mov_b32_e32 v116, 0xf149f2ca
	v_mov_b32_e32 v117, v1
	v_mov_b32_e32 v2, v1
	v_lshlrev_b32_e32 v20, 3, v4
	v_cvt_f32_ubyte0_e32 v19, v0
	v_and_b32_e32 v0, 32, v21
	s_waitcnt lgkmcnt(0)
	s_barrier
; #define tid (tid_of(wave))
; template <int mode> __device__ __forceinline__ void attn_unit(const AttnArgs& A, const int b, const int h, const int sub, char* shm, const int wave_) {
;     ...
;     const float sl = (mode == 2) ? 0.f : __builtin_amdgcn_exp2f(-8.0f * (float)(h + 1) / 11.0f) * 1.4426950408889634f * (float)dil;
;     f32x16 binit;
; #pragma unroll
;     for (int r = 0; r < 16; ++r) binit[r] = sl * (float)((r & 3) + 8 * (r >> 2) + 4 * hi);
;     const float sl32 = 32.f * sl;
;     int NT = 0;
;     if (mode == 1) { NT = 4; if (tid < 4) TL[tid] = q0 + 192 - 64 * tid; }
;     else if (mode == 3) { NT = 4; if (tid < 4) TL[tid] = gk * 256 + 192 - 64 * tid; }
;     else if (mode == 0) {
;         const int lo = q0 >= 128 ? q0 - 128 : 0; NT = (q0 + 256 - lo) / 64;
;         if (tid < NT) TL[NT - 1 - tid] = lo + 64 * tid;
;     } else {
;         NT = (q0 + 256) / 64;
;         if (tid < NT) TL[tid] = q0 + 192 - 64 * tid;
;     }
;     __syncthreads();
;     float m_reg = -1e30f, l_reg = 0.f, carry = 0.f; asm volatile("" : "+v"(m_reg), "+v"(l_reg), "+v"(carry));
;     f32x16 o[4];
; #pragma unroll
;     for (int d0 = 0; d0 < 4; ++d0) o[d0] = f32x16{};
	s_movk_i32 s0, 0x118
	v_or_b32_e32 v8, 8, v5
	v_or_b32_e32 v10, 10, v5
	v_or_b32_e32 v12, 16, v5
	v_or_b32_e32 v14, 18, v5
	v_or_b32_e32 v15, 25, v5
	v_or_b32_e32 v16, 24, v5
	v_and_or_b32 v0, v20, s0, v0
	v_lshlrev_b32_e32 v2, 4, v120
	s_movk_i32 s0, 0x70
	v_or_b32_e32 v7, 9, v5
	v_or_b32_e32 v9, 11, v5
	v_or_b32_e32 v11, 17, v5
	v_or_b32_e32 v13, 19, v5
	v_or_b32_e32 v18, 26, v5
	v_cvt_f32_ubyte0_e32 v6, v8
	v_cvt_f32_ubyte0_e32 v8, v10
	v_cvt_f32_ubyte0_e32 v10, v12
	v_cvt_f32_ubyte0_e32 v12, v14
	v_cvt_f32_ubyte0_e32 v15, v15
	v_cvt_f32_ubyte0_e32 v14, v16
	v_and_b32_e32 v3, 0x70, v2
	v_bitop3_b32 v135, v114, v2, s0 bitop3:0x78
	s_movk_i32 s0, 0x60
	s_cmp_lg_u32 0, -1
	v_or_b32_e32 v17, 27, v5
	v_cvt_f32_ubyte0_e32 v7, v7
	v_cvt_f32_ubyte0_e32 v9, v9
	v_cvt_f32_ubyte0_e32 v11, v11
	v_cvt_f32_ubyte0_e32 v13, v13
	v_cvt_f32_ubyte0_e32 v16, v18
	v_cvt_f32_ubyte0_e32 v18, v5
	v_pk_mul_f32 v[78:79], v[118:119], v[14:15] op_sel_hi:[0,1]
	v_bitop3_b32 v131, v114, v3, s0 bitop3:0x36
	s_cselect_b32 s0, 0, 0
	v_mov_b32_e32 v14, v1
	v_mov_b32_e32 v15, v1
	v_cvt_f32_ubyte0_e32 v17, v17
	v_pk_mul_f32 v[76:77], v[118:119], v[12:13] op_sel_hi:[0,1]
	v_pk_mul_f32 v[74:75], v[118:119], v[10:11] op_sel_hi:[0,1]
	v_pk_mul_f32 v[72:73], v[118:119], v[8:9] op_sel_hi:[0,1]
	v_pk_mul_f32 v[70:71], v[118:119], v[6:7] op_sel_hi:[0,1]
	v_pk_mul_f32 v[66:67], v[118:119], v[18:19] op_sel_hi:[0,1]
	v_bitop3_b32 v134, v114, v3, 32 bitop3:0x36
	v_bitop3_b32 v132, v114, v3, 64 bitop3:0x36
	v_cmp_gt_u32_e64 s[42:43], 32, v4
	v_add3_u32 v124, v22, s0, v0
	v_mov_b32_e32 v0, v1
	v_mov_b32_e32 v2, v1
	v_mov_b32_e32 v3, v1
	v_mov_b32_e32 v4, v1
	v_mov_b32_e32 v5, v1
	v_mov_b32_e32 v6, v1
	v_mov_b32_e32 v7, v1
	v_mov_b32_e32 v8, v1
	v_mov_b32_e32 v9, v1
	v_mov_b32_e32 v10, v1
	v_mov_b32_e32 v11, v1
	v_mov_b32_e32 v12, v1
	v_mov_b32_e32 v13, v1
	v_mov_b64_e32 v[64:65], v[14:15]
	v_mov_b64_e32 v[48:49], v[14:15]
	v_mov_b64_e32 v[32:33], v[14:15]
	v_pk_mul_f32 v[80:81], v[118:119], v[16:17] op_sel_hi:[0,1]
	v_mov_b64_e32 v[62:63], v[12:13]
	v_mov_b64_e32 v[60:61], v[10:11]
	v_mov_b64_e32 v[58:59], v[8:9]
	v_mov_b64_e32 v[56:57], v[6:7]
	v_mov_b64_e32 v[54:55], v[4:5]
	v_mov_b64_e32 v[52:53], v[2:3]
	v_mov_b64_e32 v[50:51], v[0:1]
	v_mov_b64_e32 v[46:47], v[12:13]
	v_mov_b64_e32 v[44:45], v[10:11]
	v_mov_b64_e32 v[42:43], v[8:9]
	v_mov_b64_e32 v[40:41], v[6:7]
	v_mov_b64_e32 v[38:39], v[4:5]
	v_mov_b64_e32 v[36:37], v[2:3]
	v_mov_b64_e32 v[34:35], v[0:1]
	v_mov_b64_e32 v[30:31], v[12:13]
	v_mov_b64_e32 v[28:29], v[10:11]
	v_mov_b64_e32 v[26:27], v[8:9]
	v_mov_b64_e32 v[24:25], v[6:7]
	v_mov_b64_e32 v[22:23], v[4:5]
	v_mov_b64_e32 v[20:21], v[2:3]
	v_mov_b64_e32 v[18:19], v[0:1]
	v_mov_b64_e32 v[16:17], v[14:15]
	v_mul_f32_e32 v129, 0x42000000, v118
	s_mov_b32 s28, 0
	v_lshlrev_b32_e32 v130, 8, v120
	v_lshl_add_u32 v115, v120, 2, s52
	s_add_i32 s29, 0, 0x20804
	v_mov_b64_e32 v[14:15], v[12:13]
	v_mov_b64_e32 v[12:13], v[10:11]
	v_mov_b64_e32 v[10:11], v[8:9]
	v_mov_b64_e32 v[8:9], v[6:7]
	v_mov_b64_e32 v[6:7], v[4:5]
	v_mov_b64_e32 v[4:5], v[2:3]
	v_mov_b64_e32 v[2:3], v[0:1]
	s_branch .LBB0_523
